# baseline (speedup 1.0000x reference)
.LBB0_35:
	s_or_b64 exec, exec, s[0:1]
	s_waitcnt vmcnt(14)
	v_mul_u32_u24_e32 v105, 0x880, v227
	s_waitcnt vmcnt(11)
	v_cvt_pk_f16_f32 v3, v150, v151
	v_cvt_pk_f16_f32 v2, v148, v149
	v_lshl_add_u32 v4, v1, 1, v105
	s_waitcnt vmcnt(10)
	v_cvt_pk_f16_f32 v1, v154, v155
	s_waitcnt lgkmcnt(0)
	v_cvt_pk_f16_f32 v0, v152, v153
	s_barrier
	v_lshl_or_b32 v233, v225, 6, v220
	v_mul_u32_u24_e32 v233, 0x110, v233
	v_add_u32_e32 v233, v233, v223
	v_add_u32_e32 v233, 0x10000, v233
	ds_read_b128 v[180:183], v233
	ds_read_b128 v[184:187], v233 offset:32
	ds_read_b128 v[188:191], v233 offset:64
	ds_read_b128 v[192:195], v233 offset:96
	ds_read_b128 v[196:199], v233 offset:128
	ds_read_b128 v[200:203], v233 offset:160
	ds_read_b128 v[204:207], v233 offset:192
	ds_read_b128 v[208:211], v233 offset:224
	ds_write2_b64 v4, v[2:3], v[0:1] offset1:34
	s_waitcnt vmcnt(9)
	v_cvt_pk_f16_f32 v1, v166, v167
	v_cvt_pk_f16_f32 v0, v164, v165
	s_waitcnt vmcnt(8)
	v_cvt_pk_f16_f32 v3, v158, v159
	v_cvt_pk_f16_f32 v2, v156, v157
	ds_write2_b64 v4, v[0:1], v[2:3] offset0:68 offset1:102
	s_waitcnt vmcnt(7)
	v_cvt_pk_f16_f32 v1, v162, v163
	v_cvt_pk_f16_f32 v0, v160, v161
	s_waitcnt vmcnt(6)
	v_cvt_pk_f16_f32 v3, v170, v171
	v_cvt_pk_f16_f32 v2, v168, v169
	ds_write2_b64 v4, v[0:1], v[2:3] offset0:136 offset1:170
	s_waitcnt vmcnt(5)
	v_cvt_pk_f16_f32 v1, v174, v175
	v_cvt_pk_f16_f32 v0, v172, v173
	s_waitcnt vmcnt(4)
	v_cvt_pk_f16_f32 v3, v178, v179
	v_cvt_pk_f16_f32 v2, v176, v177
	ds_write2_b64 v4, v[0:1], v[2:3] offset0:204 offset1:238
	ds_read_b128 v[148:151], v233 offset:8704
	ds_read_b128 v[152:155], v233 offset:8736
	ds_read_b128 v[156:159], v233 offset:8768
	ds_read_b128 v[160:163], v233 offset:8800
	ds_read_b128 v[164:167], v233 offset:8832
	ds_read_b128 v[168:171], v233 offset:8864
	ds_read_b128 v[172:175], v233 offset:8896
	ds_read_b128 v[176:179], v233 offset:8928
	v_lshlrev_b32_e32 v2, 1, v228
	s_waitcnt vmcnt(1)
	v_cvt_pk_f16_f32 v1, v40, v41
	v_cvt_pk_f16_f32 v0, v38, v39
	v_mad_u32_u24 v3, v227, s6, v2
	ds_write_b64 v3, v[0:1] offset:34816
	s_waitcnt vmcnt(0)
	v_cvt_pk_f16_f32 v1, v36, v37
	v_cvt_pk_f16_f32 v0, v34, v35
	v_mad_u32_u24 v2, v229, s6, v2
	ds_write_b64 v2, v[0:1] offset:34816
	v_mov_b32_e32 v97, 0
	v_mov_b32_e32 v0, 0
	v_mov_b32_e32 v4, 0
	v_mov_b32_e32 v96, 0
	s_and_saveexec_b64 s[0:1], vcc
	s_cbranch_execz .LBB0_37
	v_lshl_add_u32 v1, v220, 1, v230
	v_or_b32_e32 v2, 0x21000, v1
	v_add_u32_e32 v1, 0x21040, v1
	ds_read_u16 v1, v1
	ds_read_u16 v2, v2
	v_cvt_f16_f32_e32 v0, v104
	s_waitcnt lgkmcnt(1)
	v_and_b32_e32 v4, 0xffff, v1
	v_pack_b32_f16 v0, v0, 0
	s_waitcnt lgkmcnt(0)
	v_and_b32_e32 v96, 0xffff, v2
.LBB0_37:
	s_or_b64 exec, exec, s[0:1]
	v_mov_b32_e32 v98, v97
	v_mov_b32_e32 v99, v97
	v_mov_b32_e32 v5, v97
	v_mov_b32_e32 v6, v97
	v_mov_b32_e32 v7, v97
	v_mov_b32_e32 v1, v97
	v_mov_b32_e32 v2, v97
	v_mov_b32_e32 v3, v97
	s_mov_b32 s0, 0x10000
	v_or_b32_e32 v8, 0x21000, v223
	v_mfma_f32_32x32x16_f16 v[32:47], v[96:99], v[0:3], 0
	v_mfma_f32_32x32x16_f16 v[16:31], v[4:7], v[0:3], 0
	v_or_b32_e32 v114, 0x21000, v223
	v_cmp_eq_u32_e64 s[0:1], 0, v225
	s_and_b64 vcc, vcc, s[0:1]
	ds_read_b128 v[8:11], v114
	ds_read_b128 v[12:15], v114 offset:32
	ds_read_b128 v[234:237], v114 offset:64
	ds_read_b128 v[238:241], v114 offset:96
	ds_read_b128 v[242:245], v114 offset:128
	ds_read_b128 v[106:109], v114 offset:160
	ds_read_b128 v[110:113], v114 offset:192
	s_waitcnt lgkmcnt(7)
	v_mfma_f32_32x32x16_f16 v[32:47], v[180:183], v[92:95], v[32:47]
	ds_read_b128 v[0:3], v114 offset:224
	v_mfma_f32_32x32x16_f16 v[32:47], v[184:187], v[88:91], v[32:47]
	v_mfma_f32_32x32x16_f16 v[32:47], v[188:191], v[84:87], v[32:47]
	v_mfma_f32_32x32x16_f16 v[32:47], v[192:195], v[80:83], v[32:47]
	v_mfma_f32_32x32x16_f16 v[32:47], v[196:199], v[76:79], v[32:47]
	v_mfma_f32_32x32x16_f16 v[32:47], v[200:203], v[72:75], v[32:47]
	v_mfma_f32_32x32x16_f16 v[32:47], v[204:207], v[68:71], v[32:47]
	v_mfma_f32_32x32x16_f16 v[32:47], v[208:211], v[64:67], v[32:47]
	s_waitcnt lgkmcnt(0)
	v_dot2c_f32_f16_e32 v98, v92, v8
	v_mfma_f32_32x32x16_f16 v[16:31], v[148:151], v[92:95], v[16:31]
	v_dot2c_f32_f16_e32 v98, v93, v9
	v_dot2c_f32_f16_e32 v98, v94, v10
	v_dot2c_f32_f16_e32 v98, v95, v11
	v_dot2c_f32_f16_e32 v98, v88, v12
	v_mfma_f32_32x32x16_f16 v[16:31], v[152:155], v[88:91], v[16:31]
	v_dot2c_f32_f16_e32 v98, v89, v13
	v_dot2c_f32_f16_e32 v98, v90, v14
	v_dot2c_f32_f16_e32 v98, v91, v15
	v_dot2c_f32_f16_e32 v98, v84, v234
	v_mfma_f32_32x32x16_f16 v[16:31], v[156:159], v[84:87], v[16:31]
	v_dot2c_f32_f16_e32 v98, v85, v235
	v_dot2c_f32_f16_e32 v98, v86, v236
	v_dot2c_f32_f16_e32 v98, v87, v237
	v_dot2c_f32_f16_e32 v98, v80, v238
	v_mfma_f32_32x32x16_f16 v[16:31], v[160:163], v[80:83], v[16:31]
	v_dot2c_f32_f16_e32 v98, v81, v239
	v_dot2c_f32_f16_e32 v98, v82, v240
	v_dot2c_f32_f16_e32 v98, v83, v241
	v_dot2c_f32_f16_e32 v98, v76, v242
	v_mfma_f32_32x32x16_f16 v[16:31], v[164:167], v[76:79], v[16:31]
	v_dot2c_f32_f16_e32 v98, v77, v243
	v_dot2c_f32_f16_e32 v98, v78, v244
	v_dot2c_f32_f16_e32 v98, v79, v245
	v_dot2c_f32_f16_e32 v98, v72, v106
	v_mfma_f32_32x32x16_f16 v[16:31], v[168:171], v[72:75], v[16:31]
	v_dot2c_f32_f16_e32 v98, v73, v107
	v_dot2c_f32_f16_e32 v98, v74, v108
	v_dot2c_f32_f16_e32 v98, v75, v109
	v_dot2c_f32_f16_e32 v98, v68, v110
	v_mfma_f32_32x32x16_f16 v[16:31], v[172:175], v[68:71], v[16:31]
	v_dot2c_f32_f16_e32 v98, v69, v111
	v_dot2c_f32_f16_e32 v98, v70, v112
	v_dot2c_f32_f16_e32 v98, v71, v113
	v_cvt_pk_f16_f32 v7, v38, v39
	v_cvt_pk_f16_f32 v6, v36, v37
	v_cvt_pk_f16_f32 v5, v34, v35
	v_cvt_pk_f16_f32 v4, v32, v33
	v_dot2c_f32_f16_e32 v98, v64, v0
	v_dot2c_f32_f16_e32 v98, v65, v1
	v_dot2c_f32_f16_e32 v98, v66, v2
	v_mfma_f32_32x32x16_f16 v[16:31], v[176:179], v[64:67], v[16:31]
	v_dot2c_f32_f16_e32 v98, v67, v3
	v_cvt_pk_f16_f32 v35, v46, v47
	v_cvt_pk_f16_f32 v34, v44, v45
	v_cvt_pk_f16_f32 v33, v42, v43
	v_cvt_pk_f16_f32 v32, v40, v41
	ds_bpermute_b32 v36, v102, v98
	v_cvt_f32_i32_e32 v37, v226
	v_mfma_f32_32x32x16_f16 v[0:15], v[4:7], v[60:63], 0
	s_nop 3
	v_cvt_pk_f16_f32 v23, v22, v23
	v_cvt_pk_f16_f32 v22, v20, v21
	v_cvt_pk_f16_f32 v21, v18, v19
	v_cvt_pk_f16_f32 v20, v16, v17
	v_cvt_pk_f16_f32 v19, v30, v31
	v_cvt_pk_f16_f32 v18, v28, v29
	v_cvt_pk_f16_f32 v17, v26, v27
	v_mfma_f32_32x32x16_f16 v[0:15], v[32:35], v[56:59], v[0:15]
	v_cvt_pk_f16_f32 v16, v24, v25
	s_waitcnt lgkmcnt(0)
	v_add_f32_e32 v36, v98, v36
	v_cvt_f16_f32_e32 v26, v100
	v_mov_b32_e32 v98, v97
	v_lshlrev_b32_e32 v32, 6, v218
	v_mfma_f32_32x32x16_f16 v[0:15], v[20:23], v[52:55], v[0:15]
	v_fma_mixlo_f16 v20, v37, v104, v36
	v_pack_b32_f16 v20, v20, 0
	v_pack_b32_f16 v21, v26, 0
	v_cndmask_b32_e32 v96, 0, v21, vcc
	v_mfma_f32_32x32x16_f16 v[0:15], v[16:19], v[48:51], v[0:15]
	v_cndmask_b32_e32 v16, 0, v20, vcc
	v_mov_b32_e32 v17, v97
	v_mov_b32_e32 v18, v97
	v_mov_b32_e32 v19, v97
	v_cmp_ne_u32_e32 vcc, 0, v225
	s_nop 0
	v_mfma_f32_32x32x16_f16 v[0:15], v[16:19], v[96:99], v[0:15]
	s_and_saveexec_b64 s[6:7], vcc
	s_cbranch_execz .LBB0_39
	v_lshl_or_b32 v16, v222, 12, v32
	v_add_u32_e32 v16, 0x18800, v16
	s_nop 7
	ds_write_b128 v16, v[0:3]
	ds_write_b128 v16, v[4:7] offset:16
	ds_write_b128 v16, v[8:11] offset:32
	ds_write_b128 v16, v[12:15] offset:48

.LBB0_49:
	s_or_b64 exec, exec, s[6:7]
	s_waitcnt lgkmcnt(0)
	s_barrier
	s_and_saveexec_b64 s[0:1], s[4:5]
	s_cbranch_execz .LBB0_51
	v_lshl_or_b32 v0, v219, 5, v220
	v_mul_u32_u24_e32 v0, 0x110, v0
	v_or_b32_e32 v0, v0, v221
	v_add_u32_e32 v28, 0x10000, v0
	v_lshlrev_b32_e32 v29, 4, v218
	ds_read2_b64 v[16:19], v28 offset1:2
	ds_read_b128 v[48:51], v29 offset:43520
	ds_read2_b64 v[20:23], v28 offset0:4 offset1:6
	ds_read_b128 v[52:55], v29 offset:44544
	ds_read2_b64 v[24:27], v28 offset0:8 offset1:10
	ds_read_b128 v[56:59], v29 offset:45568
	ds_read2_b64 v[32:35], v28 offset0:12 offset1:14
	ds_read_b128 v[60:63], v29 offset:46592
	ds_read2_b64 v[36:39], v28 offset0:16 offset1:18
	ds_read_b128 v[64:67], v29 offset:47616
	ds_read2_b64 v[40:43], v28 offset0:20 offset1:22
	ds_read_b128 v[68:71], v29 offset:48640
	ds_read2_b64 v[44:47], v28 offset0:24 offset1:26
	ds_read_b128 v[72:75], v29 offset:49664
	ds_read2_b64 v[76:79], v28 offset0:28 offset1:30
	ds_read_b128 v[80:83], v29 offset:50688
	s_waitcnt lgkmcnt(14)
	v_mfma_f32_32x32x16_f16 v[0:15], v[16:19], v[48:51], 0
	s_waitcnt lgkmcnt(12)
	v_mfma_f32_32x32x16_f16 v[0:15], v[20:23], v[52:55], v[0:15]
	s_waitcnt lgkmcnt(10)
	v_mfma_f32_32x32x16_f16 v[0:15], v[24:27], v[56:59], v[0:15]
	s_waitcnt lgkmcnt(8)
	v_mfma_f32_32x32x16_f16 v[0:15], v[32:35], v[60:63], v[0:15]
	s_waitcnt lgkmcnt(6)
	v_mfma_f32_32x32x16_f16 v[0:15], v[36:39], v[64:67], v[0:15]
	s_waitcnt lgkmcnt(4)
	v_mfma_f32_32x32x16_f16 v[0:15], v[40:43], v[68:71], v[0:15]
	s_waitcnt lgkmcnt(2)
	v_mfma_f32_32x32x16_f16 v[0:15], v[44:47], v[72:75], v[0:15]
	v_lshl_add_u64 v[20:21], v[212:213], 4, s[34:35]
	s_waitcnt lgkmcnt(0)
	v_mfma_f32_32x32x16_f16 v[0:15], v[76:79], v[80:83], v[0:15]
	s_nop 11
	v_cvt_pk_f16_f32 v7, v6, v7
	v_cvt_pk_f16_f32 v6, v4, v5
	v_cvt_pk_f16_f32 v5, v2, v3
	v_cvt_pk_f16_f32 v4, v0, v1
	v_cvt_pk_f16_f32 v3, v14, v15
	v_cvt_pk_f16_f32 v2, v12, v13
	v_cvt_pk_f16_f32 v1, v10, v11
	v_cvt_pk_f16_f32 v0, v8, v9
	global_store_dwordx4 v[20:21], v[4:7], off
	global_store_dwordx4 v[20:21], v[0:3], off offset:16
